# V phase: merged the per-slot vmcnt waits of each 8-slot gather block into one (94 s_waitcnt removed), on top of v11
# speedup vs baseline: 1.0047x; 1.0047x over previous
.LBB0_956:
	s_and_b32 s8, s3, 0x78
	s_add_i32 s8, s8, s4
	s_ashr_i32 s9, s8, 31
	s_lshl_b64 s[10:11], s[8:9], 15
	s_add_u32 s10, s12, s10
	s_addc_u32 s11, s13, s11
	s_and_b32 s17, s16, 0x1000
	s_lshl_b32 s17, s17, 2
	s_add_u32 s10, s10, s17
	s_addc_u32 s11, s11, 0
	v_lshl_add_u64 v[54:55], s[10:11], 0, v[2:3]
	v_lshl_add_u64 v[126:127], v[54:55], 0, s[6:7]
	v_add_co_u32_e32 v128, vcc, s14, v54
	s_mov_b32 s17, s18
	s_nop 0
	v_addc_co_u32_e32 v129, vcc, 0, v55, vcc
	global_load_dword v104, v[126:127], off offset:256
	global_load_dword v106, v[126:127], off offset:512
	global_load_dword v108, v[126:127], off offset:768
	global_load_dword v110, v[126:127], off offset:1024
	global_load_dword v112, v[126:127], off offset:1280
	global_load_dword v114, v[126:127], off offset:1536
	global_load_dword v98, v[126:127], off offset:1792
	global_load_dword v100, v[126:127], off offset:2048
	global_load_dword v116, v[128:129], off offset:-4096
	global_load_dword v102, v[126:127], off offset:2304
	global_load_dword v78, v[126:127], off offset:2560
	global_load_dword v80, v[126:127], off offset:2816
	global_load_dword v82, v[126:127], off offset:3072
	global_load_dword v84, v[126:127], off offset:3328
	global_load_dword v86, v[126:127], off offset:3584
	global_load_dword v88, v[126:127], off offset:3840
	global_load_dword v90, v[128:129], off
	global_load_dword v92, v[128:129], off offset:256
	global_load_dword v94, v[128:129], off offset:512
	global_load_dword v96, v[128:129], off offset:768
	global_load_dword v76, v[128:129], off offset:1024
	global_load_dword v77, v[128:129], off offset:1280
	global_load_dword v56, v[128:129], off offset:1536
	global_load_dword v57, v[128:129], off offset:1792
	global_load_dword v58, v[128:129], off offset:2048
	global_load_dword v59, v[128:129], off offset:2304
	global_load_dword v60, v[128:129], off offset:2560
	global_load_dword v61, v[128:129], off offset:2816
	global_load_dword v62, v[128:129], off offset:3072
	global_load_dword v63, v[128:129], off offset:3328
	global_load_dword v54, v[128:129], off offset:3584
	global_load_dword v55, v[128:129], off offset:3840
	s_waitcnt vmcnt(56)
	v_and_b32_e32 v9, 0x1fff8, v64
	v_and_b32_e32 v11, 0x1fff8, v66
	v_and_b32_e32 v13, 0x1fff8, v68
	v_and_b32_e32 v15, 0x1fff8, v70
	ds_read_b64 v[126:127], v9
	ds_read_b64 v[128:129], v11
	ds_read_b64 v[130:131], v13
	ds_read_b64 v[132:133], v15
	v_and_b32_e32 v9, 0x1fff8, v72
	v_and_b32_e32 v11, 0x1fff8, v74
	v_and_b32_e32 v13, 0x1fff8, v48
	v_and_b32_e32 v15, 0x1fff8, v50
	ds_read_b64 v[134:135], v9
	ds_read_b64 v[136:137], v11
	ds_read_b64 v[138:139], v13
	ds_read_b64 v[140:141], v15
	s_setprio 1
	s_waitcnt lgkmcnt(7)
	v_cvt_pk_f32_fp8_e32 v[142:143], v126
	v_cvt_pk_f32_fp8_sdwa v[144:145], v126 src0_sel:WORD_1
	v_cvt_pk_f32_fp8_e32 v[146:147], v127
	v_cvt_pk_f32_fp8_sdwa v[126:127], v127 src0_sel:WORD_1
	s_waitcnt lgkmcnt(6)
	v_cvt_pk_f32_fp8_e32 v[148:149], v128
	v_cvt_pk_f32_fp8_sdwa v[150:151], v128 src0_sel:WORD_1
	v_cvt_pk_f32_fp8_e32 v[152:153], v129
	v_cvt_pk_f32_fp8_sdwa v[128:129], v129 src0_sel:WORD_1
	s_waitcnt lgkmcnt(5)
	v_cvt_pk_f32_fp8_e32 v[154:155], v130
	v_cvt_pk_f32_fp8_sdwa v[156:157], v130 src0_sel:WORD_1
	v_cvt_pk_f32_fp8_e32 v[158:159], v131
	v_cvt_pk_f32_fp8_sdwa v[130:131], v131 src0_sel:WORD_1
	s_waitcnt lgkmcnt(4)
	v_cvt_pk_f32_fp8_e32 v[160:161], v132
	v_cvt_pk_f32_fp8_sdwa v[162:163], v132 src0_sel:WORD_1
	v_cvt_pk_f32_fp8_e32 v[164:165], v133
	v_cvt_pk_f32_fp8_sdwa v[132:133], v133 src0_sel:WORD_1
	s_waitcnt lgkmcnt(3)
	v_cvt_pk_f32_fp8_e32 v[166:167], v134
	v_cvt_pk_f32_fp8_sdwa v[168:169], v134 src0_sel:WORD_1
	v_cvt_pk_f32_fp8_e32 v[170:171], v135
	v_cvt_pk_f32_fp8_sdwa v[134:135], v135 src0_sel:WORD_1
	s_waitcnt lgkmcnt(2)
	v_cvt_pk_f32_fp8_e32 v[172:173], v136
	v_cvt_pk_f32_fp8_sdwa v[174:175], v136 src0_sel:WORD_1
	v_cvt_pk_f32_fp8_e32 v[176:177], v137
	v_cvt_pk_f32_fp8_sdwa v[136:137], v137 src0_sel:WORD_1
	s_waitcnt lgkmcnt(1)
	v_cvt_pk_f32_fp8_e32 v[178:179], v138
	v_cvt_pk_f32_fp8_sdwa v[180:181], v138 src0_sel:WORD_1
	v_cvt_pk_f32_fp8_e32 v[182:183], v139
	v_cvt_pk_f32_fp8_sdwa v[138:139], v139 src0_sel:WORD_1
	s_waitcnt lgkmcnt(0)
	v_cvt_pk_f32_fp8_e32 v[184:185], v140
	v_cvt_pk_f32_fp8_sdwa v[186:187], v140 src0_sel:WORD_1
	v_cvt_pk_f32_fp8_e32 v[188:189], v141
	v_cvt_pk_f32_fp8_sdwa v[140:141], v141 src0_sel:WORD_1
	s_setprio 0
	s_waitcnt vmcnt(48)
	v_and_b32_e32 v9, 0x1fff8, v52
	v_and_b32_e32 v11, 0x1fff8, v32
	v_and_b32_e32 v13, 0x1fff8, v34
	v_and_b32_e32 v15, 0x1fff8, v36
	ds_read_b64 v[190:191], v9
	ds_read_b64 v[192:193], v11
	ds_read_b64 v[194:195], v13
	ds_read_b64 v[196:197], v15
	v_and_b32_e32 v9, 0x1fff8, v38
	v_and_b32_e32 v11, 0x1fff8, v40
	v_and_b32_e32 v13, 0x1fff8, v42
	v_and_b32_e32 v15, 0x1fff8, v44
	ds_read_b64 v[198:199], v9
	ds_read_b64 v[200:201], v11
	ds_read_b64 v[202:203], v13
	ds_read_b64 v[204:205], v15
	s_setprio 1
	v_pk_fma_f32 v[118:119], v[142:143], v[64:65], v[118:119] op_sel_hi:[1,0,1]
	v_pk_fma_f32 v[122:123], v[144:145], v[64:65], v[122:123] op_sel_hi:[1,0,1]
	v_pk_fma_f32 v[120:121], v[146:147], v[64:65], v[120:121] op_sel_hi:[1,0,1]
	v_pk_fma_f32 v[64:65], v[126:127], v[64:65], v[124:125] op_sel_hi:[1,0,1]
	v_pk_fma_f32 v[118:119], v[148:149], v[66:67], v[118:119] op_sel_hi:[1,0,1]
	v_pk_fma_f32 v[122:123], v[150:151], v[66:67], v[122:123] op_sel_hi:[1,0,1]
	v_pk_fma_f32 v[120:121], v[152:153], v[66:67], v[120:121] op_sel_hi:[1,0,1]
	v_pk_fma_f32 v[64:65], v[128:129], v[66:67], v[64:65] op_sel_hi:[1,0,1]
	v_pk_fma_f32 v[118:119], v[154:155], v[68:69], v[118:119] op_sel_hi:[1,0,1]
	v_pk_fma_f32 v[122:123], v[156:157], v[68:69], v[122:123] op_sel_hi:[1,0,1]
	v_pk_fma_f32 v[120:121], v[158:159], v[68:69], v[120:121] op_sel_hi:[1,0,1]
	v_pk_fma_f32 v[64:65], v[130:131], v[68:69], v[64:65] op_sel_hi:[1,0,1]
	v_pk_fma_f32 v[118:119], v[160:161], v[70:71], v[118:119] op_sel_hi:[1,0,1]
	v_pk_fma_f32 v[122:123], v[162:163], v[70:71], v[122:123] op_sel_hi:[1,0,1]
	v_pk_fma_f32 v[120:121], v[164:165], v[70:71], v[120:121] op_sel_hi:[1,0,1]
	v_pk_fma_f32 v[64:65], v[132:133], v[70:71], v[64:65] op_sel_hi:[1,0,1]
	s_waitcnt lgkmcnt(7)
	v_cvt_pk_f32_fp8_e32 v[206:207], v190
	v_cvt_pk_f32_fp8_sdwa v[208:209], v190 src0_sel:WORD_1
	v_cvt_pk_f32_fp8_e32 v[210:211], v191
	v_cvt_pk_f32_fp8_sdwa v[190:191], v191 src0_sel:WORD_1
	v_pk_fma_f32 v[118:119], v[166:167], v[72:73], v[118:119] op_sel_hi:[1,0,1]
	v_pk_fma_f32 v[122:123], v[168:169], v[72:73], v[122:123] op_sel_hi:[1,0,1]
	v_pk_fma_f32 v[120:121], v[170:171], v[72:73], v[120:121] op_sel_hi:[1,0,1]
	v_pk_fma_f32 v[64:65], v[134:135], v[72:73], v[64:65] op_sel_hi:[1,0,1]
	v_pk_fma_f32 v[118:119], v[172:173], v[74:75], v[118:119] op_sel_hi:[1,0,1]
	v_pk_fma_f32 v[122:123], v[174:175], v[74:75], v[122:123] op_sel_hi:[1,0,1]
	v_pk_fma_f32 v[120:121], v[176:177], v[74:75], v[120:121] op_sel_hi:[1,0,1]
	v_pk_fma_f32 v[64:65], v[136:137], v[74:75], v[64:65] op_sel_hi:[1,0,1]
	s_waitcnt lgkmcnt(6)
	v_cvt_pk_f32_fp8_e32 v[66:67], v192
	v_cvt_pk_f32_fp8_sdwa v[68:69], v192 src0_sel:WORD_1
	v_cvt_pk_f32_fp8_e32 v[70:71], v193
	v_cvt_pk_f32_fp8_sdwa v[72:73], v193 src0_sel:WORD_1
	s_waitcnt lgkmcnt(5)
	v_cvt_pk_f32_fp8_e32 v[74:75], v194
	v_cvt_pk_f32_fp8_sdwa v[124:125], v194 src0_sel:WORD_1
	v_pk_fma_f32 v[118:119], v[178:179], v[48:49], v[118:119] op_sel_hi:[1,0,1]
	v_pk_fma_f32 v[122:123], v[180:181], v[48:49], v[122:123] op_sel_hi:[1,0,1]
	v_pk_fma_f32 v[120:121], v[182:183], v[48:49], v[120:121] op_sel_hi:[1,0,1]
	v_pk_fma_f32 v[48:49], v[138:139], v[48:49], v[64:65] op_sel_hi:[1,0,1]
	v_pk_fma_f32 v[118:119], v[184:185], v[50:51], v[118:119] op_sel_hi:[1,0,1]
	v_pk_fma_f32 v[122:123], v[186:187], v[50:51], v[122:123] op_sel_hi:[1,0,1]
	v_pk_fma_f32 v[120:121], v[188:189], v[50:51], v[120:121] op_sel_hi:[1,0,1]
	v_pk_fma_f32 v[48:49], v[140:141], v[50:51], v[48:49] op_sel_hi:[1,0,1]
	v_pk_fma_f32 v[118:119], v[206:207], v[52:53], v[118:119] op_sel_hi:[1,0,1]
	v_pk_fma_f32 v[122:123], v[208:209], v[52:53], v[122:123] op_sel_hi:[1,0,1]
	v_pk_fma_f32 v[120:121], v[210:211], v[52:53], v[120:121] op_sel_hi:[1,0,1]
	v_pk_fma_f32 v[48:49], v[190:191], v[52:53], v[48:49] op_sel_hi:[1,0,1]
	v_cvt_pk_f32_fp8_e32 v[126:127], v195
	v_cvt_pk_f32_fp8_sdwa v[128:129], v195 src0_sel:WORD_1
	s_waitcnt lgkmcnt(4)
	v_cvt_pk_f32_fp8_e32 v[130:131], v196
	v_cvt_pk_f32_fp8_sdwa v[132:133], v196 src0_sel:WORD_1
	v_cvt_pk_f32_fp8_e32 v[134:135], v197
	v_cvt_pk_f32_fp8_sdwa v[136:137], v197 src0_sel:WORD_1
	s_waitcnt lgkmcnt(3)
	v_cvt_pk_f32_fp8_e32 v[142:143], v198
	v_cvt_pk_f32_fp8_sdwa v[144:145], v198 src0_sel:WORD_1
	v_cvt_pk_f32_fp8_e32 v[146:147], v199
	v_cvt_pk_f32_fp8_sdwa v[148:149], v199 src0_sel:WORD_1
	s_waitcnt lgkmcnt(2)
	v_cvt_pk_f32_fp8_e32 v[150:151], v200
	v_cvt_pk_f32_fp8_sdwa v[152:153], v200 src0_sel:WORD_1
	v_cvt_pk_f32_fp8_e32 v[154:155], v201
	v_cvt_pk_f32_fp8_sdwa v[156:157], v201 src0_sel:WORD_1
	s_waitcnt lgkmcnt(1)
	v_cvt_pk_f32_fp8_e32 v[158:159], v202
	v_cvt_pk_f32_fp8_sdwa v[160:161], v202 src0_sel:WORD_1
	v_cvt_pk_f32_fp8_e32 v[162:163], v203
	v_cvt_pk_f32_fp8_sdwa v[164:165], v203 src0_sel:WORD_1
	s_waitcnt lgkmcnt(0)
	v_cvt_pk_f32_fp8_e32 v[166:167], v204
	v_cvt_pk_f32_fp8_sdwa v[168:169], v204 src0_sel:WORD_1
	v_cvt_pk_f32_fp8_e32 v[170:171], v205
	v_cvt_pk_f32_fp8_sdwa v[172:173], v205 src0_sel:WORD_1
	s_setprio 0
	s_waitcnt vmcnt(40)
	v_and_b32_e32 v9, 0x1fff8, v46
	v_and_b32_e32 v11, 0x1fff8, v26
	v_and_b32_e32 v13, 0x1fff8, v28
	v_and_b32_e32 v15, 0x1fff8, v30
	ds_read_b64 v[50:51], v9
	ds_read_b64 v[52:53], v11
	ds_read_b64 v[64:65], v13
	ds_read_b64 v[138:139], v15
	v_and_b32_e32 v9, 0x1fff8, v4
	v_and_b32_e32 v11, 0x1fff8, v6
	v_and_b32_e32 v13, 0x1fff8, v8
	v_and_b32_e32 v15, 0x1fff8, v10
	ds_read_b64 v[140:141], v9
	ds_read_b64 v[174:175], v11
	ds_read_b64 v[176:177], v13
	ds_read_b64 v[178:179], v15
	s_setprio 1
	v_pk_fma_f32 v[66:67], v[66:67], v[32:33], v[118:119] op_sel_hi:[1,0,1]
	v_pk_fma_f32 v[68:69], v[68:69], v[32:33], v[122:123] op_sel_hi:[1,0,1]
	v_pk_fma_f32 v[70:71], v[70:71], v[32:33], v[120:121] op_sel_hi:[1,0,1]
	v_pk_fma_f32 v[32:33], v[72:73], v[32:33], v[48:49] op_sel_hi:[1,0,1]
	v_pk_fma_f32 v[66:67], v[74:75], v[34:35], v[66:67] op_sel_hi:[1,0,1]
	v_pk_fma_f32 v[68:69], v[124:125], v[34:35], v[68:69] op_sel_hi:[1,0,1]
	v_pk_fma_f32 v[70:71], v[126:127], v[34:35], v[70:71] op_sel_hi:[1,0,1]
	v_pk_fma_f32 v[32:33], v[128:129], v[34:35], v[32:33] op_sel_hi:[1,0,1]
	v_pk_fma_f32 v[66:67], v[130:131], v[36:37], v[66:67] op_sel_hi:[1,0,1]
	v_pk_fma_f32 v[68:69], v[132:133], v[36:37], v[68:69] op_sel_hi:[1,0,1]
	v_pk_fma_f32 v[70:71], v[134:135], v[36:37], v[70:71] op_sel_hi:[1,0,1]
	v_pk_fma_f32 v[32:33], v[136:137], v[36:37], v[32:33] op_sel_hi:[1,0,1]
	s_waitcnt lgkmcnt(7)
	v_cvt_pk_f32_fp8_e32 v[180:181], v50
	v_cvt_pk_f32_fp8_sdwa v[182:183], v50 src0_sel:WORD_1
	v_cvt_pk_f32_fp8_e32 v[184:185], v51
	v_cvt_pk_f32_fp8_sdwa v[50:51], v51 src0_sel:WORD_1
	v_pk_fma_f32 v[66:67], v[142:143], v[38:39], v[66:67] op_sel_hi:[1,0,1]
	v_pk_fma_f32 v[68:69], v[144:145], v[38:39], v[68:69] op_sel_hi:[1,0,1]
	v_pk_fma_f32 v[70:71], v[146:147], v[38:39], v[70:71] op_sel_hi:[1,0,1]
	v_pk_fma_f32 v[32:33], v[148:149], v[38:39], v[32:33] op_sel_hi:[1,0,1]
	s_waitcnt lgkmcnt(6)
	v_cvt_pk_f32_fp8_e32 v[186:187], v52
	v_cvt_pk_f32_fp8_sdwa v[188:189], v52 src0_sel:WORD_1
	v_cvt_pk_f32_fp8_e32 v[190:191], v53
	v_cvt_pk_f32_fp8_sdwa v[52:53], v53 src0_sel:WORD_1
	v_pk_fma_f32 v[66:67], v[150:151], v[40:41], v[66:67] op_sel_hi:[1,0,1]
	v_pk_fma_f32 v[68:69], v[152:153], v[40:41], v[68:69] op_sel_hi:[1,0,1]
	v_pk_fma_f32 v[70:71], v[154:155], v[40:41], v[70:71] op_sel_hi:[1,0,1]
	v_pk_fma_f32 v[32:33], v[156:157], v[40:41], v[32:33] op_sel_hi:[1,0,1]
	s_waitcnt lgkmcnt(5)
	v_cvt_pk_f32_fp8_e32 v[192:193], v64
	v_cvt_pk_f32_fp8_sdwa v[194:195], v64 src0_sel:WORD_1
	v_cvt_pk_f32_fp8_e32 v[196:197], v65
	v_cvt_pk_f32_fp8_sdwa v[64:65], v65 src0_sel:WORD_1
	v_pk_fma_f32 v[66:67], v[158:159], v[42:43], v[66:67] op_sel_hi:[1,0,1]
	v_pk_fma_f32 v[68:69], v[160:161], v[42:43], v[68:69] op_sel_hi:[1,0,1]
	v_pk_fma_f32 v[70:71], v[162:163], v[42:43], v[70:71] op_sel_hi:[1,0,1]
	v_pk_fma_f32 v[32:33], v[164:165], v[42:43], v[32:33] op_sel_hi:[1,0,1]
	s_waitcnt lgkmcnt(4)
	v_cvt_pk_f32_fp8_e32 v[198:199], v138
	v_cvt_pk_f32_fp8_sdwa v[200:201], v138 src0_sel:WORD_1
	v_cvt_pk_f32_fp8_e32 v[202:203], v139
	v_cvt_pk_f32_fp8_sdwa v[138:139], v139 src0_sel:WORD_1
	v_pk_fma_f32 v[66:67], v[166:167], v[44:45], v[66:67] op_sel_hi:[1,0,1]
	v_pk_fma_f32 v[68:69], v[168:169], v[44:45], v[68:69] op_sel_hi:[1,0,1]
	v_pk_fma_f32 v[70:71], v[170:171], v[44:45], v[70:71] op_sel_hi:[1,0,1]
	v_pk_fma_f32 v[32:33], v[172:173], v[44:45], v[32:33] op_sel_hi:[1,0,1]
	v_pk_fma_f32 v[66:67], v[180:181], v[46:47], v[66:67] op_sel_hi:[1,0,1]
	v_pk_fma_f32 v[68:69], v[182:183], v[46:47], v[68:69] op_sel_hi:[1,0,1]
	v_pk_fma_f32 v[70:71], v[184:185], v[46:47], v[70:71] op_sel_hi:[1,0,1]
	v_pk_fma_f32 v[32:33], v[50:51], v[46:47], v[32:33] op_sel_hi:[1,0,1]
	s_waitcnt lgkmcnt(3)
	v_cvt_pk_f32_fp8_e32 v[34:35], v140
	v_cvt_pk_f32_fp8_sdwa v[36:37], v140 src0_sel:WORD_1
	v_cvt_pk_f32_fp8_e32 v[38:39], v141
	v_cvt_pk_f32_fp8_sdwa v[40:41], v141 src0_sel:WORD_1
	s_waitcnt lgkmcnt(2)
	v_cvt_pk_f32_fp8_e32 v[42:43], v174
	v_cvt_pk_f32_fp8_sdwa v[44:45], v174 src0_sel:WORD_1
	v_cvt_pk_f32_fp8_e32 v[46:47], v175
	v_cvt_pk_f32_fp8_sdwa v[48:49], v175 src0_sel:WORD_1
	s_waitcnt lgkmcnt(1)
	v_cvt_pk_f32_fp8_e32 v[50:51], v176
	v_cvt_pk_f32_fp8_sdwa v[72:73], v176 src0_sel:WORD_1
	v_cvt_pk_f32_fp8_e32 v[74:75], v177
	v_cvt_pk_f32_fp8_sdwa v[118:119], v177 src0_sel:WORD_1
	s_waitcnt lgkmcnt(0)
	v_cvt_pk_f32_fp8_e32 v[120:121], v178
	v_cvt_pk_f32_fp8_sdwa v[122:123], v178 src0_sel:WORD_1
	v_cvt_pk_f32_fp8_e32 v[124:125], v179
	v_pk_fma_f32 v[66:67], v[186:187], v[26:27], v[66:67] op_sel_hi:[1,0,1]
	v_pk_fma_f32 v[68:69], v[188:189], v[26:27], v[68:69] op_sel_hi:[1,0,1]
	v_pk_fma_f32 v[70:71], v[190:191], v[26:27], v[70:71] op_sel_hi:[1,0,1]
	v_pk_fma_f32 v[26:27], v[52:53], v[26:27], v[32:33] op_sel_hi:[1,0,1]
	v_pk_fma_f32 v[66:67], v[192:193], v[28:29], v[66:67] op_sel_hi:[1,0,1]
	v_pk_fma_f32 v[68:69], v[194:195], v[28:29], v[68:69] op_sel_hi:[1,0,1]
	v_pk_fma_f32 v[70:71], v[196:197], v[28:29], v[70:71] op_sel_hi:[1,0,1]
	v_pk_fma_f32 v[26:27], v[64:65], v[28:29], v[26:27] op_sel_hi:[1,0,1]
	v_pk_fma_f32 v[66:67], v[198:199], v[30:31], v[66:67] op_sel_hi:[1,0,1]
	v_pk_fma_f32 v[68:69], v[200:201], v[30:31], v[68:69] op_sel_hi:[1,0,1]
	v_pk_fma_f32 v[70:71], v[202:203], v[30:31], v[70:71] op_sel_hi:[1,0,1]
	v_pk_fma_f32 v[26:27], v[138:139], v[30:31], v[26:27] op_sel_hi:[1,0,1]
	v_cvt_pk_f32_fp8_sdwa v[126:127], v179 src0_sel:WORD_1
	s_setprio 0
	s_waitcnt vmcnt(32)
	v_and_b32_e32 v9, 0x1fff8, v14
	v_and_b32_e32 v11, 0x1fff8, v18
	v_and_b32_e32 v13, 0x1fff8, v20
	v_and_b32_e32 v15, 0x1fff8, v22
	ds_read_b64 v[28:29], v9
	ds_read_b64 v[30:31], v11
	ds_read_b64 v[32:33], v13
	ds_read_b64 v[52:53], v15
	v_and_b32_e32 v9, 0x1fff8, v24
	v_and_b32_e32 v11, 0x1fff8, v12
	v_and_b32_e32 v13, 0x1fff8, v16
	v_and_b32_e32 v15, 0x1fff8, v7
	ds_read_b64 v[64:65], v9
	ds_read_b64 v[128:129], v11
	ds_read_b64 v[130:131], v13
	ds_read_b64 v[132:133], v15
	s_setprio 1
	s_waitcnt lgkmcnt(7)
	v_cvt_pk_f32_fp8_e32 v[134:135], v28
	v_pk_fma_f32 v[34:35], v[34:35], v[4:5], v[66:67] op_sel_hi:[1,0,1]
	s_waitcnt lgkmcnt(6)
	v_cvt_pk_f32_fp8_e32 v[140:141], v30
	v_pk_fma_f32 v[34:35], v[42:43], v[6:7], v[34:35] op_sel_hi:[1,0,1]
	s_waitcnt lgkmcnt(5)
	v_cvt_pk_f32_fp8_e32 v[146:147], v32
	v_pk_fma_f32 v[34:35], v[50:51], v[8:9], v[34:35] op_sel_hi:[1,0,1]
	s_waitcnt lgkmcnt(4)
	v_cvt_pk_f32_fp8_e32 v[152:153], v52
	v_pk_fma_f32 v[34:35], v[120:121], v[10:11], v[34:35] op_sel_hi:[1,0,1]
	s_waitcnt lgkmcnt(3)
	v_cvt_pk_f32_fp8_e32 v[158:159], v64
	v_pk_fma_f32 v[34:35], v[134:135], v[14:15], v[34:35] op_sel_hi:[1,0,1]
	s_waitcnt lgkmcnt(2)
	v_cvt_pk_f32_fp8_e32 v[164:165], v128
	v_pk_fma_f32 v[34:35], v[140:141], v[18:19], v[34:35] op_sel_hi:[1,0,1]
	s_waitcnt lgkmcnt(1)
	v_cvt_pk_f32_fp8_e32 v[170:171], v130
	v_pk_fma_f32 v[34:35], v[146:147], v[20:21], v[34:35] op_sel_hi:[1,0,1]
	v_cvt_pk_f32_fp8_sdwa v[136:137], v28 src0_sel:WORD_1
	v_pk_fma_f32 v[34:35], v[152:153], v[22:23], v[34:35] op_sel_hi:[1,0,1]
	v_cvt_pk_f32_fp8_sdwa v[142:143], v30 src0_sel:WORD_1
	v_pk_fma_f32 v[34:35], v[158:159], v[24:25], v[34:35] op_sel_hi:[1,0,1]
	v_cvt_pk_f32_fp8_sdwa v[148:149], v32 src0_sel:WORD_1
	v_pk_fma_f32 v[34:35], v[164:165], v[12:13], v[34:35] op_sel_hi:[1,0,1]
	v_cvt_pk_f32_fp8_sdwa v[154:155], v52 src0_sel:WORD_1
	v_pk_fma_f32 v[120:121], v[170:171], v[16:17], v[34:35] op_sel_hi:[1,0,1]
	v_pk_fma_f32 v[34:35], v[36:37], v[4:5], v[68:69] op_sel_hi:[1,0,1]
	v_cvt_pk_f32_fp8_sdwa v[160:161], v64 src0_sel:WORD_1
	v_pk_fma_f32 v[34:35], v[44:45], v[6:7], v[34:35] op_sel_hi:[1,0,1]
	v_cvt_pk_f32_fp8_sdwa v[166:167], v128 src0_sel:WORD_1
	v_pk_fma_f32 v[34:35], v[72:73], v[8:9], v[34:35] op_sel_hi:[1,0,1]
	v_cvt_pk_f32_fp8_sdwa v[172:173], v130 src0_sel:WORD_1
	v_pk_fma_f32 v[34:35], v[122:123], v[10:11], v[34:35] op_sel_hi:[1,0,1]
	v_cvt_pk_f32_fp8_e32 v[138:139], v29
	v_pk_fma_f32 v[34:35], v[136:137], v[14:15], v[34:35] op_sel_hi:[1,0,1]
	v_cvt_pk_f32_fp8_sdwa v[28:29], v29 src0_sel:WORD_1
	v_pk_fma_f32 v[34:35], v[142:143], v[18:19], v[34:35] op_sel_hi:[1,0,1]
	v_cvt_pk_f32_fp8_e32 v[144:145], v31
	v_pk_fma_f32 v[34:35], v[148:149], v[20:21], v[34:35] op_sel_hi:[1,0,1]
	v_pk_fma_f32 v[26:27], v[40:41], v[4:5], v[26:27] op_sel_hi:[1,0,1]
	v_pk_fma_f32 v[34:35], v[154:155], v[22:23], v[34:35] op_sel_hi:[1,0,1]
	v_cvt_pk_f32_fp8_sdwa v[30:31], v31 src0_sel:WORD_1
	v_pk_fma_f32 v[34:35], v[160:161], v[24:25], v[34:35] op_sel_hi:[1,0,1]
	v_cvt_pk_f32_fp8_e32 v[150:151], v33
	v_pk_fma_f32 v[34:35], v[166:167], v[12:13], v[34:35] op_sel_hi:[1,0,1]
	v_pk_fma_f32 v[26:27], v[48:49], v[6:7], v[26:27] op_sel_hi:[1,0,1]
	v_pk_fma_f32 v[122:123], v[172:173], v[16:17], v[34:35] op_sel_hi:[1,0,1]
	v_pk_fma_f32 v[34:35], v[38:39], v[4:5], v[70:71] op_sel_hi:[1,0,1]
	v_cvt_pk_f32_fp8_sdwa v[32:33], v33 src0_sel:WORD_1
	v_pk_fma_f32 v[34:35], v[46:47], v[6:7], v[34:35] op_sel_hi:[1,0,1]
	v_cvt_pk_f32_fp8_e32 v[156:157], v53
	v_pk_fma_f32 v[34:35], v[74:75], v[8:9], v[34:35] op_sel_hi:[1,0,1]
	v_pk_fma_f32 v[8:9], v[118:119], v[8:9], v[26:27] op_sel_hi:[1,0,1]
	v_pk_fma_f32 v[34:35], v[124:125], v[10:11], v[34:35] op_sel_hi:[1,0,1]
	v_cvt_pk_f32_fp8_sdwa v[52:53], v53 src0_sel:WORD_1
	v_cvt_pk_f32_fp8_e32 v[162:163], v65
	v_pk_fma_f32 v[34:35], v[138:139], v[14:15], v[34:35] op_sel_hi:[1,0,1]
	v_pk_fma_f32 v[8:9], v[126:127], v[10:11], v[8:9] op_sel_hi:[1,0,1]
	v_cvt_pk_f32_fp8_sdwa v[64:65], v65 src0_sel:WORD_1
	v_cvt_pk_f32_fp8_e32 v[168:169], v129
	v_pk_fma_f32 v[34:35], v[144:145], v[18:19], v[34:35] op_sel_hi:[1,0,1]
	v_pk_fma_f32 v[8:9], v[28:29], v[14:15], v[8:9] op_sel_hi:[1,0,1]
	v_cvt_pk_f32_fp8_sdwa v[128:129], v129 src0_sel:WORD_1
	v_cvt_pk_f32_fp8_e32 v[174:175], v131
	v_pk_fma_f32 v[34:35], v[150:151], v[20:21], v[34:35] op_sel_hi:[1,0,1]
	v_pk_fma_f32 v[8:9], v[30:31], v[18:19], v[8:9] op_sel_hi:[1,0,1]
	v_cvt_pk_f32_fp8_sdwa v[130:131], v131 src0_sel:WORD_1
	v_pk_fma_f32 v[34:35], v[156:157], v[22:23], v[34:35] op_sel_hi:[1,0,1]
	v_pk_fma_f32 v[8:9], v[32:33], v[20:21], v[8:9] op_sel_hi:[1,0,1]
	s_waitcnt lgkmcnt(0)
	v_cvt_pk_f32_fp8_e32 v[118:119], v132
	v_pk_fma_f32 v[34:35], v[162:163], v[24:25], v[34:35] op_sel_hi:[1,0,1]
	v_pk_fma_f32 v[8:9], v[52:53], v[22:23], v[8:9] op_sel_hi:[1,0,1]
	v_pk_fma_f32 v[34:35], v[168:169], v[12:13], v[34:35] op_sel_hi:[1,0,1]
	v_pk_fma_f32 v[8:9], v[64:65], v[24:25], v[8:9] op_sel_hi:[1,0,1]
	v_pk_fma_f32 v[124:125], v[174:175], v[16:17], v[34:35] op_sel_hi:[1,0,1]
	v_pk_fma_f32 v[8:9], v[128:129], v[12:13], v[8:9] op_sel_hi:[1,0,1]
	v_cvt_pk_f32_fp8_sdwa v[126:127], v132 src0_sel:WORD_1
	v_cvt_pk_f32_fp8_e32 v[134:135], v133
	v_cvt_pk_f32_fp8_sdwa v[132:133], v133 src0_sel:WORD_1
	v_pk_fma_f32 v[128:129], v[130:131], v[16:17], v[8:9] op_sel_hi:[1,0,1]
	v_mov_b32_e32 v130, v7
	s_setprio 0
	s_add_i32 s18, s18, 2
	s_cmp_gt_u32 s17, 61
	s_cselect_b64 s[10:11], -1, 0
	s_cmp_lt_u32 s17, 62
	s_cselect_b32 s19, s18, 63
	s_lshl_b32 s20, s19, 1
	s_and_b32 s20, s20, 0xf8
	s_add_i32 s20, s20, s4
	s_ashr_i32 s21, s20, 31
	s_lshl_b64 s[20:21], s[20:21], 15
	s_add_u32 s20, s12, s20
	s_addc_u32 s21, s13, s21
	s_lshl_b32 s19, s19, 13
	s_and_b32 s19, s19, 0x6000
	s_add_u32 s20, s20, s19
	s_addc_u32 s21, s21, 0
	v_lshl_add_u64 v[6:7], s[20:21], 0, v[2:3]
	v_add_co_u32_e32 v136, vcc, s5, v6
	global_load_dword v64, v[6:7], off
	global_load_dword v66, v[6:7], off offset:256
	global_load_dword v68, v[6:7], off offset:512
	global_load_dword v70, v[6:7], off offset:768
	global_load_dword v72, v[6:7], off offset:1024
	global_load_dword v74, v[6:7], off offset:1280
	global_load_dword v48, v[6:7], off offset:1536
	global_load_dword v50, v[6:7], off offset:1792
	global_load_dword v52, v[6:7], off offset:2048
	global_load_dword v32, v[6:7], off offset:2304
	global_load_dword v34, v[6:7], off offset:2560
	global_load_dword v36, v[6:7], off offset:2816
	global_load_dword v38, v[6:7], off offset:3072
	global_load_dword v40, v[6:7], off offset:3328
	global_load_dword v42, v[6:7], off offset:3584
	global_load_dword v44, v[6:7], off offset:3840
	v_addc_co_u32_e32 v137, vcc, 0, v7, vcc
	global_load_dword v46, v[136:137], off
	global_load_dword v26, v[136:137], off offset:256
	global_load_dword v28, v[136:137], off offset:512
	global_load_dword v30, v[136:137], off offset:768
	global_load_dword v4, v[136:137], off offset:1024
	global_load_dword v6, v[136:137], off offset:1280
	global_load_dword v8, v[136:137], off offset:1536
	global_load_dword v10, v[136:137], off offset:1792
	global_load_dword v14, v[136:137], off offset:2048
	global_load_dword v18, v[136:137], off offset:2304
	global_load_dword v20, v[136:137], off offset:2560
	global_load_dword v22, v[136:137], off offset:2816
	global_load_dword v24, v[136:137], off offset:3072
	global_load_dword v12, v[136:137], off offset:3328
	global_load_dword v16, v[136:137], off offset:3584
	global_load_dword v7, v[136:137], off offset:3840
	s_waitcnt vmcnt(55)
	v_and_b32_e32 v9, 0x1fff8, v116
	v_and_b32_e32 v11, 0x1fff8, v104
	v_and_b32_e32 v13, 0x1fff8, v106
	v_and_b32_e32 v15, 0x1fff8, v108
	ds_read_b64 v[136:137], v9
	ds_read_b64 v[138:139], v11
	ds_read_b64 v[140:141], v13
	ds_read_b64 v[142:143], v15
	v_and_b32_e32 v9, 0x1fff8, v110
	v_and_b32_e32 v11, 0x1fff8, v112
	v_and_b32_e32 v13, 0x1fff8, v114
	v_and_b32_e32 v15, 0x1fff8, v98
	ds_read_b64 v[144:145], v9
	ds_read_b64 v[146:147], v11
	ds_read_b64 v[148:149], v13
	ds_read_b64 v[150:151], v15
	s_setprio 1
	s_waitcnt lgkmcnt(7)
	v_cvt_pk_f32_fp8_e32 v[152:153], v136
	v_cvt_pk_f32_fp8_sdwa v[154:155], v136 src0_sel:WORD_1
	v_cvt_pk_f32_fp8_e32 v[156:157], v137
	v_cvt_pk_f32_fp8_sdwa v[136:137], v137 src0_sel:WORD_1
	s_waitcnt lgkmcnt(6)
	v_cvt_pk_f32_fp8_e32 v[158:159], v138
	v_cvt_pk_f32_fp8_sdwa v[160:161], v138 src0_sel:WORD_1
	v_cvt_pk_f32_fp8_e32 v[162:163], v139
	v_cvt_pk_f32_fp8_sdwa v[138:139], v139 src0_sel:WORD_1
	s_waitcnt lgkmcnt(5)
	v_cvt_pk_f32_fp8_e32 v[164:165], v140
	v_cvt_pk_f32_fp8_sdwa v[166:167], v140 src0_sel:WORD_1
	v_cvt_pk_f32_fp8_e32 v[168:169], v141
	v_cvt_pk_f32_fp8_sdwa v[140:141], v141 src0_sel:WORD_1
	s_waitcnt lgkmcnt(4)
	v_cvt_pk_f32_fp8_e32 v[170:171], v142
	v_cvt_pk_f32_fp8_sdwa v[172:173], v142 src0_sel:WORD_1
	v_cvt_pk_f32_fp8_e32 v[174:175], v143
	v_cvt_pk_f32_fp8_sdwa v[142:143], v143 src0_sel:WORD_1
	s_waitcnt lgkmcnt(3)
	v_cvt_pk_f32_fp8_e32 v[176:177], v144
	v_cvt_pk_f32_fp8_sdwa v[178:179], v144 src0_sel:WORD_1
	v_cvt_pk_f32_fp8_e32 v[180:181], v145
	v_cvt_pk_f32_fp8_sdwa v[144:145], v145 src0_sel:WORD_1
	s_waitcnt lgkmcnt(2)
	v_cvt_pk_f32_fp8_e32 v[182:183], v146
	v_cvt_pk_f32_fp8_sdwa v[184:185], v146 src0_sel:WORD_1
	v_cvt_pk_f32_fp8_e32 v[186:187], v147
	v_cvt_pk_f32_fp8_sdwa v[146:147], v147 src0_sel:WORD_1
	s_waitcnt lgkmcnt(1)
	v_cvt_pk_f32_fp8_e32 v[188:189], v148
	v_cvt_pk_f32_fp8_sdwa v[190:191], v148 src0_sel:WORD_1
	v_cvt_pk_f32_fp8_e32 v[192:193], v149
	v_cvt_pk_f32_fp8_sdwa v[148:149], v149 src0_sel:WORD_1
	s_waitcnt lgkmcnt(0)
	v_cvt_pk_f32_fp8_e32 v[194:195], v150
	v_cvt_pk_f32_fp8_sdwa v[196:197], v150 src0_sel:WORD_1
	v_cvt_pk_f32_fp8_e32 v[198:199], v151
	v_cvt_pk_f32_fp8_sdwa v[150:151], v151 src0_sel:WORD_1
	s_setprio 0
	v_and_b32_e32 v9, 0x1fff8, v100
	s_waitcnt vmcnt(48)
	v_and_b32_e32 v11, 0x1fff8, v102
	v_and_b32_e32 v13, 0x1fff8, v78
	v_and_b32_e32 v15, 0x1fff8, v80
	ds_read_b64 v[200:201], v9
	ds_read_b64 v[202:203], v11
	ds_read_b64 v[204:205], v13
	ds_read_b64 v[206:207], v15
	v_and_b32_e32 v9, 0x1fff8, v82
	v_and_b32_e32 v11, 0x1fff8, v84
	v_and_b32_e32 v13, 0x1fff8, v86
	v_and_b32_e32 v15, 0x1fff8, v88
	ds_read_b64 v[208:209], v9
	ds_read_b64 v[210:211], v11
	ds_read_b64 v[212:213], v13
	ds_read_b64 v[214:215], v15
	s_setprio 1
	v_pk_fma_f32 v[118:119], v[118:119], v[130:131], v[120:121] op_sel_hi:[1,0,1]
	v_pk_fma_f32 v[120:121], v[126:127], v[130:131], v[122:123] op_sel_hi:[1,0,1]
	v_pk_fma_f32 v[122:123], v[134:135], v[130:131], v[124:125] op_sel_hi:[1,0,1]
	v_pk_fma_f32 v[118:119], v[152:153], v[116:117], v[118:119] op_sel_hi:[1,0,1]
	v_pk_fma_f32 v[120:121], v[154:155], v[116:117], v[120:121] op_sel_hi:[1,0,1]
	v_pk_fma_f32 v[122:123], v[156:157], v[116:117], v[122:123] op_sel_hi:[1,0,1]
	v_pk_fma_f32 v[124:125], v[132:133], v[130:131], v[128:129] op_sel_hi:[1,0,1]
	v_pk_fma_f32 v[118:119], v[158:159], v[104:105], v[118:119] op_sel_hi:[1,0,1]
	v_pk_fma_f32 v[120:121], v[160:161], v[104:105], v[120:121] op_sel_hi:[1,0,1]
	v_pk_fma_f32 v[122:123], v[162:163], v[104:105], v[122:123] op_sel_hi:[1,0,1]
	v_pk_fma_f32 v[116:117], v[136:137], v[116:117], v[124:125] op_sel_hi:[1,0,1]
	v_pk_fma_f32 v[118:119], v[164:165], v[106:107], v[118:119] op_sel_hi:[1,0,1]
	v_pk_fma_f32 v[120:121], v[166:167], v[106:107], v[120:121] op_sel_hi:[1,0,1]
	v_pk_fma_f32 v[122:123], v[168:169], v[106:107], v[122:123] op_sel_hi:[1,0,1]
	v_pk_fma_f32 v[104:105], v[138:139], v[104:105], v[116:117] op_sel_hi:[1,0,1]
	v_pk_fma_f32 v[118:119], v[170:171], v[108:109], v[118:119] op_sel_hi:[1,0,1]
	v_pk_fma_f32 v[120:121], v[172:173], v[108:109], v[120:121] op_sel_hi:[1,0,1]
	v_pk_fma_f32 v[122:123], v[174:175], v[108:109], v[122:123] op_sel_hi:[1,0,1]
	v_pk_fma_f32 v[104:105], v[140:141], v[106:107], v[104:105] op_sel_hi:[1,0,1]
	s_waitcnt lgkmcnt(7)
	v_cvt_pk_f32_fp8_e32 v[216:217], v200
	v_cvt_pk_f32_fp8_sdwa v[218:219], v200 src0_sel:WORD_1
	v_cvt_pk_f32_fp8_e32 v[220:221], v201
	v_pk_fma_f32 v[118:119], v[176:177], v[110:111], v[118:119] op_sel_hi:[1,0,1]
	v_pk_fma_f32 v[120:121], v[178:179], v[110:111], v[120:121] op_sel_hi:[1,0,1]
	v_pk_fma_f32 v[122:123], v[180:181], v[110:111], v[122:123] op_sel_hi:[1,0,1]
	v_pk_fma_f32 v[104:105], v[142:143], v[108:109], v[104:105] op_sel_hi:[1,0,1]
	v_cvt_pk_f32_fp8_sdwa v[200:201], v201 src0_sel:WORD_1
	s_waitcnt lgkmcnt(6)
	v_cvt_pk_f32_fp8_e32 v[222:223], v202
	v_cvt_pk_f32_fp8_sdwa v[224:225], v202 src0_sel:WORD_1
	v_cvt_pk_f32_fp8_e32 v[226:227], v203
	v_pk_fma_f32 v[118:119], v[182:183], v[112:113], v[118:119] op_sel_hi:[1,0,1]
	v_pk_fma_f32 v[120:121], v[184:185], v[112:113], v[120:121] op_sel_hi:[1,0,1]
	v_pk_fma_f32 v[122:123], v[186:187], v[112:113], v[122:123] op_sel_hi:[1,0,1]
	v_pk_fma_f32 v[104:105], v[144:145], v[110:111], v[104:105] op_sel_hi:[1,0,1]
	v_cvt_pk_f32_fp8_sdwa v[202:203], v203 src0_sel:WORD_1
	v_pk_fma_f32 v[118:119], v[188:189], v[114:115], v[118:119] op_sel_hi:[1,0,1]
	v_pk_fma_f32 v[120:121], v[190:191], v[114:115], v[120:121] op_sel_hi:[1,0,1]
	v_pk_fma_f32 v[122:123], v[192:193], v[114:115], v[122:123] op_sel_hi:[1,0,1]
	v_pk_fma_f32 v[104:105], v[146:147], v[112:113], v[104:105] op_sel_hi:[1,0,1]
	s_waitcnt lgkmcnt(4)
	v_cvt_pk_f32_fp8_e32 v[124:125], v207
	v_pk_fma_f32 v[118:119], v[194:195], v[98:99], v[118:119] op_sel_hi:[1,0,1]
	v_pk_fma_f32 v[120:121], v[196:197], v[98:99], v[120:121] op_sel_hi:[1,0,1]
	v_pk_fma_f32 v[122:123], v[198:199], v[98:99], v[122:123] op_sel_hi:[1,0,1]
	v_pk_fma_f32 v[104:105], v[148:149], v[114:115], v[104:105] op_sel_hi:[1,0,1]
	v_pk_fma_f32 v[118:119], v[216:217], v[100:101], v[118:119] op_sel_hi:[1,0,1]
	v_pk_fma_f32 v[120:121], v[218:219], v[100:101], v[120:121] op_sel_hi:[1,0,1]
	v_pk_fma_f32 v[122:123], v[220:221], v[100:101], v[122:123] op_sel_hi:[1,0,1]
	v_pk_fma_f32 v[98:99], v[150:151], v[98:99], v[104:105] op_sel_hi:[1,0,1]
	v_pk_fma_f32 v[118:119], v[222:223], v[102:103], v[118:119] op_sel_hi:[1,0,1]
	v_pk_fma_f32 v[120:121], v[224:225], v[102:103], v[120:121] op_sel_hi:[1,0,1]
	v_pk_fma_f32 v[122:123], v[226:227], v[102:103], v[122:123] op_sel_hi:[1,0,1]
	v_pk_fma_f32 v[98:99], v[200:201], v[100:101], v[98:99] op_sel_hi:[1,0,1]
	v_cvt_pk_f32_fp8_e32 v[106:107], v204
	v_cvt_pk_f32_fp8_sdwa v[108:109], v204 src0_sel:WORD_1
	v_cvt_pk_f32_fp8_e32 v[110:111], v205
	v_cvt_pk_f32_fp8_sdwa v[112:113], v205 src0_sel:WORD_1
	v_cvt_pk_f32_fp8_e32 v[114:115], v206
	v_cvt_pk_f32_fp8_sdwa v[116:117], v206 src0_sel:WORD_1
	v_cvt_pk_f32_fp8_sdwa v[126:127], v207 src0_sel:WORD_1
	s_waitcnt lgkmcnt(3)
	v_cvt_pk_f32_fp8_e32 v[128:129], v208
	v_cvt_pk_f32_fp8_sdwa v[130:131], v208 src0_sel:WORD_1
	v_cvt_pk_f32_fp8_e32 v[132:133], v209
	v_cvt_pk_f32_fp8_sdwa v[134:135], v209 src0_sel:WORD_1
	s_waitcnt lgkmcnt(2)
	v_cvt_pk_f32_fp8_e32 v[136:137], v210
	v_cvt_pk_f32_fp8_sdwa v[138:139], v210 src0_sel:WORD_1
	v_cvt_pk_f32_fp8_e32 v[140:141], v211
	v_cvt_pk_f32_fp8_sdwa v[142:143], v211 src0_sel:WORD_1
	s_waitcnt lgkmcnt(1)
	v_cvt_pk_f32_fp8_e32 v[144:145], v212
	v_cvt_pk_f32_fp8_sdwa v[146:147], v212 src0_sel:WORD_1
	v_cvt_pk_f32_fp8_e32 v[148:149], v213
	v_cvt_pk_f32_fp8_sdwa v[152:153], v213 src0_sel:WORD_1
	s_waitcnt lgkmcnt(0)
	v_cvt_pk_f32_fp8_e32 v[154:155], v214
	v_cvt_pk_f32_fp8_sdwa v[156:157], v214 src0_sel:WORD_1
	v_cvt_pk_f32_fp8_e32 v[158:159], v215
	v_cvt_pk_f32_fp8_sdwa v[160:161], v215 src0_sel:WORD_1
	v_pk_fma_f32 v[98:99], v[202:203], v[102:103], v[98:99] op_sel_hi:[1,0,1]
	s_setprio 0
	s_waitcnt vmcnt(40)
	v_and_b32_e32 v9, 0x1fff8, v90
	v_and_b32_e32 v11, 0x1fff8, v92
	v_and_b32_e32 v13, 0x1fff8, v94
	v_and_b32_e32 v15, 0x1fff8, v96
	ds_read_b64 v[100:101], v9
	ds_read_b64 v[102:103], v11
	ds_read_b64 v[104:105], v13
	ds_read_b64 v[150:151], v15
	v_and_b32_e32 v9, 0x1fff8, v76
	v_and_b32_e32 v11, 0x1fff8, v77
	v_and_b32_e32 v13, 0x1fff8, v56
	v_and_b32_e32 v15, 0x1fff8, v57
	ds_read_b64 v[162:163], v9
	ds_read_b64 v[164:165], v11
	ds_read_b64 v[166:167], v13
	ds_read_b64 v[168:169], v15
	s_setprio 1
	v_pk_fma_f32 v[106:107], v[106:107], v[78:79], v[118:119] op_sel_hi:[1,0,1]
	v_pk_fma_f32 v[108:109], v[108:109], v[78:79], v[120:121] op_sel_hi:[1,0,1]
	v_pk_fma_f32 v[110:111], v[110:111], v[78:79], v[122:123] op_sel_hi:[1,0,1]
	v_pk_fma_f32 v[78:79], v[112:113], v[78:79], v[98:99] op_sel_hi:[1,0,1]
	v_pk_fma_f32 v[106:107], v[114:115], v[80:81], v[106:107] op_sel_hi:[1,0,1]
	v_pk_fma_f32 v[108:109], v[116:117], v[80:81], v[108:109] op_sel_hi:[1,0,1]
	v_pk_fma_f32 v[110:111], v[124:125], v[80:81], v[110:111] op_sel_hi:[1,0,1]
	v_pk_fma_f32 v[78:79], v[126:127], v[80:81], v[78:79] op_sel_hi:[1,0,1]
	s_waitcnt lgkmcnt(7)
	v_cvt_pk_f32_fp8_e32 v[170:171], v100
	v_cvt_pk_f32_fp8_sdwa v[172:173], v100 src0_sel:WORD_1
	v_cvt_pk_f32_fp8_e32 v[174:175], v101
	v_cvt_pk_f32_fp8_sdwa v[100:101], v101 src0_sel:WORD_1
	v_pk_fma_f32 v[106:107], v[128:129], v[82:83], v[106:107] op_sel_hi:[1,0,1]
	v_pk_fma_f32 v[108:109], v[130:131], v[82:83], v[108:109] op_sel_hi:[1,0,1]
	v_pk_fma_f32 v[110:111], v[132:133], v[82:83], v[110:111] op_sel_hi:[1,0,1]
	v_pk_fma_f32 v[78:79], v[134:135], v[82:83], v[78:79] op_sel_hi:[1,0,1]
	s_waitcnt lgkmcnt(6)
	v_cvt_pk_f32_fp8_e32 v[176:177], v102
	v_cvt_pk_f32_fp8_sdwa v[178:179], v102 src0_sel:WORD_1
	v_cvt_pk_f32_fp8_e32 v[180:181], v103
	v_cvt_pk_f32_fp8_sdwa v[102:103], v103 src0_sel:WORD_1
	v_pk_fma_f32 v[106:107], v[136:137], v[84:85], v[106:107] op_sel_hi:[1,0,1]
	v_pk_fma_f32 v[108:109], v[138:139], v[84:85], v[108:109] op_sel_hi:[1,0,1]
	v_pk_fma_f32 v[110:111], v[140:141], v[84:85], v[110:111] op_sel_hi:[1,0,1]
	v_pk_fma_f32 v[78:79], v[142:143], v[84:85], v[78:79] op_sel_hi:[1,0,1]
	s_waitcnt lgkmcnt(5)
	v_cvt_pk_f32_fp8_e32 v[182:183], v104
	v_cvt_pk_f32_fp8_sdwa v[184:185], v104 src0_sel:WORD_1
	v_cvt_pk_f32_fp8_e32 v[186:187], v105
	v_cvt_pk_f32_fp8_sdwa v[104:105], v105 src0_sel:WORD_1
	v_pk_fma_f32 v[106:107], v[144:145], v[86:87], v[106:107] op_sel_hi:[1,0,1]
	v_pk_fma_f32 v[108:109], v[146:147], v[86:87], v[108:109] op_sel_hi:[1,0,1]
	v_pk_fma_f32 v[110:111], v[148:149], v[86:87], v[110:111] op_sel_hi:[1,0,1]
	v_pk_fma_f32 v[78:79], v[152:153], v[86:87], v[78:79] op_sel_hi:[1,0,1]
	v_pk_fma_f32 v[106:107], v[154:155], v[88:89], v[106:107] op_sel_hi:[1,0,1]
	v_pk_fma_f32 v[108:109], v[156:157], v[88:89], v[108:109] op_sel_hi:[1,0,1]
	v_pk_fma_f32 v[110:111], v[158:159], v[88:89], v[110:111] op_sel_hi:[1,0,1]
	v_pk_fma_f32 v[78:79], v[160:161], v[88:89], v[78:79] op_sel_hi:[1,0,1]
	s_waitcnt lgkmcnt(3)
	v_cvt_pk_f32_fp8_e32 v[194:195], v162
	v_cvt_pk_f32_fp8_sdwa v[196:197], v162 src0_sel:WORD_1
	v_cvt_pk_f32_fp8_e32 v[198:199], v163
	v_cvt_pk_f32_fp8_sdwa v[162:163], v163 src0_sel:WORD_1
	s_waitcnt lgkmcnt(2)
	v_cvt_pk_f32_fp8_e32 v[200:201], v164
	v_cvt_pk_f32_fp8_sdwa v[202:203], v164 src0_sel:WORD_1
	v_cvt_pk_f32_fp8_e32 v[204:205], v165
	v_cvt_pk_f32_fp8_sdwa v[164:165], v165 src0_sel:WORD_1
	v_pk_fma_f32 v[106:107], v[170:171], v[90:91], v[106:107] op_sel_hi:[1,0,1]
	v_pk_fma_f32 v[108:109], v[172:173], v[90:91], v[108:109] op_sel_hi:[1,0,1]
	v_pk_fma_f32 v[110:111], v[174:175], v[90:91], v[110:111] op_sel_hi:[1,0,1]
	v_pk_fma_f32 v[78:79], v[100:101], v[90:91], v[78:79] op_sel_hi:[1,0,1]
	v_pk_fma_f32 v[106:107], v[176:177], v[92:93], v[106:107] op_sel_hi:[1,0,1]
	v_pk_fma_f32 v[108:109], v[178:179], v[92:93], v[108:109] op_sel_hi:[1,0,1]
	v_pk_fma_f32 v[110:111], v[180:181], v[92:93], v[110:111] op_sel_hi:[1,0,1]
	v_pk_fma_f32 v[78:79], v[102:103], v[92:93], v[78:79] op_sel_hi:[1,0,1]
	v_cvt_pk_f32_fp8_e32 v[188:189], v150
	v_cvt_pk_f32_fp8_sdwa v[190:191], v150 src0_sel:WORD_1
	v_cvt_pk_f32_fp8_e32 v[192:193], v151
	v_cvt_pk_f32_fp8_sdwa v[150:151], v151 src0_sel:WORD_1
	v_pk_fma_f32 v[106:107], v[182:183], v[94:95], v[106:107] op_sel_hi:[1,0,1]
	v_pk_fma_f32 v[108:109], v[184:185], v[94:95], v[108:109] op_sel_hi:[1,0,1]
	v_pk_fma_f32 v[110:111], v[186:187], v[94:95], v[110:111] op_sel_hi:[1,0,1]
	v_pk_fma_f32 v[78:79], v[104:105], v[94:95], v[78:79] op_sel_hi:[1,0,1]
	s_waitcnt lgkmcnt(1)
	v_cvt_pk_f32_fp8_sdwa v[88:89], v167 src0_sel:WORD_1
	s_waitcnt lgkmcnt(0)
	v_cvt_pk_f32_fp8_sdwa v[94:95], v169 src0_sel:WORD_1
	v_mov_b32_e32 v116, v163
	v_mov_b32_e32 v117, v165
	v_pk_mul_f32 v[114:115], v[162:163], v[76:77]
	v_pk_mul_f32 v[116:117], v[116:117], v[76:77]
	v_pk_fma_f32 v[106:107], v[188:189], v[96:97], v[106:107] op_sel_hi:[1,0,1]
	v_pk_fma_f32 v[108:109], v[190:191], v[96:97], v[108:109] op_sel_hi:[1,0,1]
	v_pk_fma_f32 v[110:111], v[192:193], v[96:97], v[110:111] op_sel_hi:[1,0,1]
	v_pk_fma_f32 v[78:79], v[150:151], v[96:97], v[78:79] op_sel_hi:[1,0,1]
	v_mov_b32_e32 v115, v116
	v_mov_b32_e32 v80, v77
	v_pk_mul_f32 v[98:99], v[88:89], v[56:57]
	v_mov_b32_e32 v88, v89
	v_mov_b32_e32 v89, v95
	v_mov_b32_e32 v100, v57
	v_pk_fma_f32 v[106:107], v[194:195], v[76:77], v[106:107] op_sel_hi:[1,0,1]
	v_pk_fma_f32 v[108:109], v[196:197], v[76:77], v[108:109] op_sel_hi:[1,0,1]
	v_pk_fma_f32 v[110:111], v[198:199], v[76:77], v[110:111] op_sel_hi:[1,0,1]
	v_pk_add_f32 v[78:79], v[78:79], v[114:115]
	v_mov_b32_e32 v76, v77
	v_pk_mul_f32 v[80:81], v[164:165], v[80:81]
	v_cvt_pk_f32_fp8_e32 v[82:83], v166
	v_cvt_pk_f32_fp8_sdwa v[84:85], v166 src0_sel:WORD_1
	v_cvt_pk_f32_fp8_e32 v[86:87], v167
	v_cvt_pk_f32_fp8_e32 v[90:91], v168
	v_cvt_pk_f32_fp8_sdwa v[92:93], v168 src0_sel:WORD_1
	v_cvt_pk_f32_fp8_e32 v[96:97], v169
	v_pk_mul_f32 v[88:89], v[88:89], v[56:57]
	v_pk_mul_f32 v[94:95], v[94:95], v[100:101]
	s_setprio 0
	s_waitcnt vmcnt(32)
	v_and_b32_e32 v9, 0x1fff8, v58
	v_and_b32_e32 v11, 0x1fff8, v59
	v_and_b32_e32 v13, 0x1fff8, v60
	v_and_b32_e32 v15, 0x1fff8, v61
	ds_read_b64 v[100:101], v9
	ds_read_b64 v[102:103], v11
	ds_read_b64 v[104:105], v13
	ds_read_b64 v[112:113], v15
	v_and_b32_e32 v9, 0x1fff8, v62
	v_and_b32_e32 v11, 0x1fff8, v63
	v_and_b32_e32 v13, 0x1fff8, v54
	v_and_b32_e32 v15, 0x1fff8, v55
	ds_read_b64 v[114:115], v9
	ds_read_b64 v[118:119], v11
	ds_read_b64 v[120:121], v13
	ds_read_b64 v[122:123], v15
	s_setprio 1
	s_waitcnt lgkmcnt(7)
	v_cvt_pk_f32_fp8_e32 v[124:125], v100
	v_cvt_pk_f32_fp8_sdwa v[126:127], v100 src0_sel:WORD_1
	v_cvt_pk_f32_fp8_e32 v[128:129], v101
	v_cvt_pk_f32_fp8_sdwa v[100:101], v101 src0_sel:WORD_1
	s_waitcnt lgkmcnt(6)
	v_cvt_pk_f32_fp8_sdwa v[134:135], v103 src0_sel:WORD_1
	v_cvt_pk_f32_fp8_e32 v[130:131], v102
	s_waitcnt lgkmcnt(5)
	v_cvt_pk_f32_fp8_e32 v[138:139], v104
	v_cvt_pk_f32_fp8_sdwa v[140:141], v104 src0_sel:WORD_1
	v_cvt_pk_f32_fp8_e32 v[142:143], v105
	v_cvt_pk_f32_fp8_sdwa v[104:105], v105 src0_sel:WORD_1
	s_waitcnt lgkmcnt(4)
	v_cvt_pk_f32_fp8_sdwa v[148:149], v113 src0_sel:WORD_1
	v_pk_fma_f32 v[106:107], v[200:201], v[76:77], v[106:107] op_sel_hi:[1,0,1]
	s_waitcnt lgkmcnt(3)
	v_cvt_pk_f32_fp8_e32 v[152:153], v114
	v_cvt_pk_f32_fp8_sdwa v[154:155], v114 src0_sel:WORD_1
	v_cvt_pk_f32_fp8_e32 v[156:157], v115
	v_cvt_pk_f32_fp8_sdwa v[114:115], v115 src0_sel:WORD_1
	s_waitcnt lgkmcnt(2)
	v_cvt_pk_f32_fp8_sdwa v[162:163], v119 src0_sel:WORD_1
	v_pk_fma_f32 v[82:83], v[82:83], v[56:57], v[106:107] op_sel_hi:[1,0,1]
	v_mov_b32_e32 v106, v57
	v_mov_b32_e32 v116, v59
	v_cvt_pk_f32_fp8_e32 v[144:145], v112
	v_cvt_pk_f32_fp8_e32 v[158:159], v118
	v_cvt_pk_f32_fp8_sdwa v[160:161], v118 src0_sel:WORD_1
	v_cvt_pk_f32_fp8_e32 v[164:165], v119
	s_waitcnt lgkmcnt(1)
	v_cvt_pk_f32_fp8_e32 v[118:119], v120
	v_cvt_pk_f32_fp8_sdwa v[168:169], v120 src0_sel:WORD_1
	v_cvt_pk_f32_fp8_e32 v[170:171], v121
	v_cvt_pk_f32_fp8_sdwa v[120:121], v121 src0_sel:WORD_1
	s_waitcnt lgkmcnt(0)
; #define GAS __attribute__((address_space(1)))
; __device__ __forceinline__ unsigned f2bf(float f) { unsigned u = __builtin_bit_cast(unsigned, f); return (u + 0x7fffu + ((u >> 16) & 1u)) >> 16; }
; template <int VVAR> __device__ __forceinline__ void peer_v_phase(LAS unsigned char* lds, int wave, int vcu, const unsigned char* __restrict__ VS_l, const unsigned* __restrict__ PW, bf16* __restrict__ Y) {
;     ...
; #pragma unroll 1
;     for (int it = 0; it < (VVAR == 5 ? 2 : 64); it += 2) {
;         V_HALF(pa, pb, it + 1);
;         V_HALF(pb, pa, it + 2);
;         if ((it & 3) == 2) {
;             const int blk = th * 128 + wave + 8 * (it >> 2);
;             bf16* yp = Y + ((size_t)blk * 1024 + cs * 8) * 64 + lane;
; #pragma unroll
;             for (int c = 0; c < 8; ++c) ((GAS unsigned short*)yp)[c * 64] = (unsigned short)f2bf(acc[c]);
; #pragma unroll
;             for (int c = 0; c < 8; ++c) acc[c] = 0.f;
	v_cvt_pk_f32_fp8_sdwa v[176:177], v123 src0_sel:WORD_1
	v_pk_fma_f32 v[82:83], v[90:91], v[106:107], v[82:83] op_sel_hi:[1,0,1]
	v_pk_mul_f32 v[136:137], v[100:101], v[58:59]
	v_mov_b32_e32 v100, v101
	v_mov_b32_e32 v101, v135
	v_pk_mul_f32 v[134:135], v[134:135], v[116:117]
	v_mov_b32_e32 v116, v61
	v_pk_fma_f32 v[82:83], v[124:125], v[58:59], v[82:83] op_sel_hi:[1,0,1]
	v_mov_b32_e32 v90, v59
	v_pk_mul_f32 v[150:151], v[104:105], v[60:61]
	v_mov_b32_e32 v104, v105
	v_mov_b32_e32 v105, v149
	v_pk_mul_f32 v[148:149], v[148:149], v[116:117]
	v_mov_b32_e32 v116, v63
	v_pk_fma_f32 v[82:83], v[130:131], v[90:91], v[82:83] op_sel_hi:[1,0,1]
	v_pk_mul_f32 v[166:167], v[114:115], v[62:63]
	v_mov_b32_e32 v114, v115
	v_mov_b32_e32 v115, v163
	v_pk_mul_f32 v[162:163], v[162:163], v[116:117]
	v_pk_fma_f32 v[82:83], v[138:139], v[60:61], v[82:83] op_sel_hi:[1,0,1]
	v_mov_b32_e32 v116, v61
	v_cvt_pk_f32_fp8_e32 v[172:173], v122
	v_pk_mul_f32 v[180:181], v[120:121], v[54:55]
	v_mov_b32_e32 v120, v121
	v_mov_b32_e32 v121, v177
	v_pk_fma_f32 v[82:83], v[144:145], v[116:117], v[82:83] op_sel_hi:[1,0,1]
	v_pk_mul_f32 v[182:183], v[120:121], v[54:55]
	v_pk_fma_f32 v[82:83], v[152:153], v[62:63], v[82:83] op_sel_hi:[1,0,1]
	v_mov_b32_e32 v120, v63
	v_pk_fma_f32 v[82:83], v[158:159], v[120:121], v[82:83] op_sel_hi:[1,0,1]
	v_mov_b32_e32 v124, v55
	v_pk_fma_f32 v[82:83], v[118:119], v[54:55], v[82:83] op_sel_hi:[1,0,1]
	v_cvt_pk_f32_fp8_sdwa v[132:133], v102 src0_sel:WORD_1
	v_cvt_pk_f32_fp8_e32 v[102:103], v103
	v_pk_fma_f32 v[118:119], v[172:173], v[124:125], v[82:83] op_sel_hi:[1,0,1]
	v_pk_fma_f32 v[82:83], v[202:203], v[76:77], v[108:109] op_sel_hi:[1,0,1]
	v_pk_fma_f32 v[76:77], v[204:205], v[76:77], v[110:111] op_sel_hi:[1,0,1]
	v_pk_fma_f32 v[82:83], v[84:85], v[56:57], v[82:83] op_sel_hi:[1,0,1]
	v_pk_fma_f32 v[56:57], v[86:87], v[56:57], v[76:77] op_sel_hi:[1,0,1]
	v_cvt_pk_f32_fp8_sdwa v[146:147], v112 src0_sel:WORD_1
	v_cvt_pk_f32_fp8_e32 v[112:113], v113
	v_pk_fma_f32 v[56:57], v[96:97], v[106:107], v[56:57] op_sel_hi:[1,0,1]
	v_pk_fma_f32 v[82:83], v[92:93], v[106:107], v[82:83] op_sel_hi:[1,0,1]
	v_pk_fma_f32 v[56:57], v[128:129], v[58:59], v[56:57] op_sel_hi:[1,0,1]
	v_pk_fma_f32 v[82:83], v[126:127], v[58:59], v[82:83] op_sel_hi:[1,0,1]
	v_pk_fma_f32 v[56:57], v[102:103], v[90:91], v[56:57] op_sel_hi:[1,0,1]
	v_cvt_pk_f32_fp8_e32 v[178:179], v123
	v_pk_fma_f32 v[56:57], v[142:143], v[60:61], v[56:57] op_sel_hi:[1,0,1]
	v_pk_fma_f32 v[82:83], v[132:133], v[90:91], v[82:83] op_sel_hi:[1,0,1]
	v_pk_fma_f32 v[56:57], v[112:113], v[116:117], v[56:57] op_sel_hi:[1,0,1]
	v_pk_fma_f32 v[82:83], v[140:141], v[60:61], v[82:83] op_sel_hi:[1,0,1]
	v_pk_fma_f32 v[56:57], v[156:157], v[62:63], v[56:57] op_sel_hi:[1,0,1]
	v_pk_fma_f32 v[82:83], v[146:147], v[116:117], v[82:83] op_sel_hi:[1,0,1]
	v_pk_fma_f32 v[56:57], v[164:165], v[120:121], v[56:57] op_sel_hi:[1,0,1]
	v_pk_fma_f32 v[82:83], v[154:155], v[62:63], v[82:83] op_sel_hi:[1,0,1]
	v_pk_fma_f32 v[56:57], v[170:171], v[54:55], v[56:57] op_sel_hi:[1,0,1]
	v_mov_b32_e32 v81, v117
	v_pk_fma_f32 v[82:83], v[160:161], v[120:121], v[82:83] op_sel_hi:[1,0,1]
	v_pk_fma_f32 v[120:121], v[178:179], v[124:125], v[56:57] op_sel_hi:[1,0,1]
	v_pk_add_f32 v[56:57], v[78:79], v[80:81]
	v_mov_b32_e32 v99, v88
	v_pk_mul_f32 v[100:101], v[100:101], v[58:59]
	v_pk_add_f32 v[56:57], v[56:57], v[98:99]
	v_mov_b32_e32 v95, v89
	v_pk_add_f32 v[56:57], v[56:57], v[94:95]
	v_mov_b32_e32 v137, v100
	v_pk_mul_f32 v[104:105], v[104:105], v[60:61]
	v_pk_add_f32 v[56:57], v[56:57], v[136:137]
	v_mov_b32_e32 v135, v101
	v_pk_add_f32 v[56:57], v[56:57], v[134:135]
	v_mov_b32_e32 v151, v104
	v_pk_mul_f32 v[114:115], v[114:115], v[62:63]
	v_pk_add_f32 v[56:57], v[56:57], v[150:151]
	v_mov_b32_e32 v149, v105
	v_cvt_pk_f32_fp8_sdwa v[174:175], v122 src0_sel:WORD_1
	v_pk_add_f32 v[56:57], v[56:57], v[148:149]
	v_mov_b32_e32 v167, v114
	v_pk_fma_f32 v[82:83], v[168:169], v[54:55], v[82:83] op_sel_hi:[1,0,1]
	v_mov_b32_e32 v54, v55
	v_pk_add_f32 v[56:57], v[56:57], v[166:167]
	v_mov_b32_e32 v163, v115
	v_pk_mul_f32 v[54:55], v[176:177], v[54:55]
	v_pk_add_f32 v[56:57], v[56:57], v[162:163]
	v_mov_b32_e32 v181, v182
	v_pk_add_f32 v[56:57], v[56:57], v[180:181]
	v_mov_b32_e32 v55, v183
	v_pk_fma_f32 v[122:123], v[174:175], v[124:125], v[82:83] op_sel_hi:[1,0,1]
	v_pk_add_f32 v[124:125], v[56:57], v[54:55]
	s_setprio 0
	s_bitcmp0_b32 s17, 1
	s_cbranch_scc1 .LBB0_955
	s_lshl_b64 s[8:9], s[8:9], 17
	v_bfe_u32 v9, v118, 16, 1
	v_lshl_add_u64 v[54:55], v[0:1], 0, s[8:9]
	v_add3_u32 v9, v118, v9, s15
	global_store_short_d16_hi v[54:55], v9, off
	v_bfe_u32 v9, v119, 16, 1
	v_add3_u32 v9, v119, v9, s15
	global_store_short_d16_hi v[54:55], v9, off offset:128
	v_bfe_u32 v9, v122, 16, 1
	v_add3_u32 v9, v122, v9, s15
	global_store_short_d16_hi v[54:55], v9, off offset:256
	v_bfe_u32 v9, v123, 16, 1
	v_add3_u32 v9, v123, v9, s15
	global_store_short_d16_hi v[54:55], v9, off offset:384
	v_bfe_u32 v9, v120, 16, 1
	v_add3_u32 v9, v120, v9, s15
	global_store_short_d16_hi v[54:55], v9, off offset:512
	v_bfe_u32 v9, v121, 16, 1
	v_add3_u32 v9, v121, v9, s15
	global_store_short_d16_hi v[54:55], v9, off offset:640
	v_bfe_u32 v9, v124, 16, 1
	v_add3_u32 v9, v124, v9, s15
	global_store_short_d16_hi v[54:55], v9, off offset:768
	v_bfe_u32 v9, v125, 16, 1
	v_mov_b32_e32 v118, 0
	v_add3_u32 v9, v125, v9, s15
	v_mov_b32_e32 v119, v118
	v_mov_b32_e32 v122, v118
	v_mov_b32_e32 v123, v118
	v_mov_b32_e32 v120, v118
	v_mov_b32_e32 v121, v118
	v_mov_b32_e32 v124, v118
	v_mov_b32_e32 v125, v118
	global_store_short_d16_hi v[54:55], v9, off offset:896
	s_branch .LBB0_955
